# strategy 7.4: one static s_setprio 1 for waves 4-7 at attention phase entry (dense + neighbourhood attention), reset to 0 at the out-proj entry
# baseline (speedup 1.0000x reference)
.LBB0_720:
	v_readlane_b32 s0, v254, 60
	s_add_i32 s2, s0, 4
	v_readlane_b32 s4, v253, 4
	v_readlane_b32 s5, v253, 5
	s_cmp_gt_i32 s4, s2
	s_cselect_b64 s[0:1], -1, 0
	s_cmp_ge_i32 s2, s5
	s_cselect_b64 s[2:3], -1, 0
	s_or_b64 s[0:1], s[0:1], s[2:3]
	s_and_b64 vcc, exec, s[0:1]
	v_readlane_b32 s6, v253, 6
	v_readlane_b32 s7, v253, 7
	s_cbranch_vccnz .LBB0_1097
	s_cmp_ge_u32 s56, 4
	s_cbranch_scc0 .Lattn_prio_done
	s_setprio 1
.Lattn_prio_done:
	s_lshl_b32 s12, s56, 10
	s_cmp_lg_u32 0, -1
	s_cselect_b32 s0, 0, 0
	s_lshl_b32 s2, s56, 3
	s_ashr_i32 s3, s2, 31
	v_writelane_b32 v255, s2, 8
	s_lshl_b32 s6, s56, 5
	s_add_i32 s34, s12, s0
	v_writelane_b32 v255, s3, 9
	s_andn2_b32 s2, s2, 31
	s_ashr_i32 s3, s2, 31
	s_ashr_i32 s7, s6, 31
	s_lshl_b32 s0, s56, 8
	s_lshl_b32 s1, s56, 4
	v_writelane_b32 v255, s2, 10
	s_and_b32 s8, s1, 48
	s_add_i32 s33, s0, 0
	v_writelane_b32 v255, s3, 11
	s_lshl_b64 s[0:1], s[6:7], 11
	v_writelane_b32 v255, s0, 12
	s_add_i32 s35, s34, 0x6000
	v_readlane_b32 s16, v253, 8
	v_writelane_b32 v255, s1, 13
	s_mul_i32 s0, s56, 0xf00
	s_add_i32 s7, s33, s0
	v_readlane_b32 s0, v254, 61
	s_cmpk_gt_i32 s0, 0x47f
	s_mul_i32 s0, s56, 0x24000
	v_writelane_b32 v255, s0, 3
	s_mul_hi_i32 s0, s6, 0x1200
	v_readlane_b32 s17, v253, 9
	v_readlane_b32 s22, v253, 14
	v_readlane_b32 s23, v253, 15
	v_writelane_b32 v255, s0, 14
	s_mov_b64 s[16:17], s[22:23]
	v_readlane_b32 s18, v253, 10
	v_readlane_b32 s19, v253, 11
	v_readlane_b32 s20, v253, 12
	v_readlane_b32 s21, v253, 13
	v_mbcnt_lo_u32_b32 v0, -1, 0
	v_mbcnt_hi_u32_b32 v0, -1, v0
	s_cbranch_scc1 .LBB0_803
	s_add_u32 s0, s16, 0x6400000
	s_addc_u32 s1, s17, 0
	s_mul_i32 s2, s56, 0x24000
	s_add_u32 s2, s0, s2
	s_mul_hi_i32 s3, s6, 0x1200
	v_mov_b64_e32 v[2:3], s[0:1]
	s_movk_i32 s9, 0x1200
	s_addc_u32 s3, s1, s3
	v_mad_i64_i32 v[4:5], s[0:1], v0, s9, v[2:3]
	v_readlane_b32 s0, v255, 8
	v_readlane_b32 s1, v255, 9
	s_lshl_b64 s[4:5], s[0:1], 1
	v_lshl_add_u64 v[202:203], v[4:5], 0, s[4:5]
	v_ashrrev_i32_e32 v4, 2, v0
	s_waitcnt vmcnt(0)
	v_add_u32_e32 v7, s8, v4
	v_mad_i64_i32 v[4:5], s[0:1], v7, s9, 0
	v_mad_i64_i32 v[2:3], s[0:1], v7, s9, v[2:3]
	v_readlane_b32 s0, v255, 10
	v_readlane_b32 s1, v255, 11
	v_lshlrev_b32_e32 v7, 3, v0
	s_lshl_b64 s[10:11], s[0:1], 1
	v_and_b32_e32 v7, 24, v7
	v_lshl_add_u64 v[2:3], v[2:3], 0, s[10:11]
	v_lshlrev_b32_e32 v114, 1, v7
	s_cmp_lg_u32 0, -1
	v_lshl_add_u64 v[204:205], v[2:3], 0, v[114:115]
	v_lshlrev_b32_e32 v2, 1, v0
	s_cselect_b32 s0, 0, 0
	v_ashrrev_i32_e32 v6, 5, v0
	v_and_b32_e32 v2, 32, v2
	s_addk_i32 s0, 0x6000
	v_lshlrev_b32_e32 v9, 4, v0
	v_add_u32_e32 v8, s0, v2
	v_and_b32_e32 v3, 0xc0, v9
	v_add_u32_e32 v13, 0, v2
	v_lshlrev_b32_e32 v2, 3, v6
	v_and_b32_e32 v1, 31, v0
	v_lshl_or_b32 v10, v6, 8, v3
	v_ashrrev_i32_e32 v3, 31, v2
	v_mul_u32_u24_e32 v14, 0x900, v1
	v_lshl_add_u64 v[2:3], v[2:3], 1, s[2:3]
	v_readlane_b32 s2, v255, 12
	v_lshlrev_b32_e32 v114, 1, v14
	v_readlane_b32 s3, v255, 13
	s_add_u32 s2, s16, s2
	v_lshlrev_b32_e32 v12, 4, v1
	v_lshl_add_u64 v[206:207], v[2:3], 0, v[114:115]
	v_lshl_add_u32 v246, v1, 2, s33
	v_lshlrev_b32_e32 v2, 9, v6
	v_lshlrev_b32_e32 v1, 1, v1
	s_addc_u32 s3, s17, s3
	v_and_b32_e32 v114, 0x70, v9
	v_lshlrev_b32_e32 v11, 10, v6
	v_add3_u32 v244, v8, v7, v10
	v_add3_u32 v245, v13, v7, v10
	v_lshlrev_b32_e32 v247, 4, v6
	v_add3_u32 v249, s7, v2, v1
	v_ashrrev_i32_e32 v2, 3, v0
	v_lshl_add_u64 v[6:7], s[2:3], 0, v[114:115]
	s_mov_b64 s[2:3], 0x13000000
	v_lshl_add_u64 v[208:209], v[6:7], 0, s[2:3]
	v_add_u32_e32 v6, 8, v2
	v_ashrrev_i32_e32 v3, 31, v2
	v_ashrrev_i32_e32 v7, 31, v6
	v_lshlrev_b32_e32 v8, 7, v2
	v_lshlrev_b64 v[210:211], 11, v[2:3]
	v_lshlrev_b32_e32 v9, 7, v6
	v_lshlrev_b64 v[212:213], 11, v[6:7]
	v_add_u32_e32 v6, 16, v2
	v_add_u32_e32 v2, 24, v2
	v_ashrrev_i32_e32 v7, 31, v6
	v_ashrrev_i32_e32 v3, 31, v2
	v_lshlrev_b32_e32 v10, 7, v6
	v_lshlrev_b64 v[214:215], 11, v[6:7]
	v_lshlrev_b32_e32 v6, 7, v2
	v_lshlrev_b64 v[216:217], 11, v[2:3]
	v_and_b32_e32 v2, 3, v0
	v_lshl_or_b32 v4, v2, 4, v4
	v_mov_b64_e32 v[2:3], s[4:5]
	v_add_u32_e32 v1, s7, v114
	v_lshl_add_u64 v[218:219], v[4:5], 0, s[10:11]
	v_mad_i64_i32 v[220:221], s[2:3], v0, s9, v[2:3]
	v_add3_u32 v65, 0, v11, v12
	v_cmp_gt_u32_e64 s[0:1], 32, v0
	v_lshl_add_u32 v248, v0, 2, s33
	v_lshl_add_u64 v[222:223], s[16:17], 0, v[218:219]
	v_lshl_add_u64 v[224:225], s[16:17], 0, v[220:221]
	v_add_u32_e32 v114, v1, v8
	v_add_u32_e32 v250, v1, v9
	v_add_u32_e32 v251, v1, v10
	v_add_u32_e32 v252, v1, v6
	v_readlane_b32 s10, v254, 61
	s_branch .LBB0_724

.LBB0_1097:
	s_setprio 0
	v_readlane_b32 s0, v255, 5
	v_readlane_b32 s1, v255, 6
	s_and_b64 vcc, exec, s[0:1]
	s_cbranch_vccz .LBB0_1099
	s_waitcnt lgkmcnt(0)
